# speedup vs baseline: 1.0011x; 1.0004x over previous
_Z9ln_kernelPKfPfS0_S0_:
	s_load_dwordx8 s[4:11], s[0:1], 0x0
	s_and_b32 s3, s2, 7
	s_lshl_b32 s3, s3, 8
	s_lshr_b32 s2, s2, 3
	s_or_b32 s2, s2, s3
	s_mov_b32 s3, 0
	s_lshl_b64 s[2:3], s[2:3], 14
	v_mov_b32_e32 v51, 0
	v_lshlrev_b32_e32 v50, 4, v0
	s_waitcnt lgkmcnt(0)
	s_add_u32 s0, s4, s2
	s_addc_u32 s1, s5, s3
	s_movk_i32 s4, 0x2000
	v_lshl_add_u64 v[2:3], s[0:1], 0, v[50:51]
	v_add_co_u32_e32 v4, vcc, s4, v2
	global_load_dwordx4 v[34:37], v50, s[0:1] nt
	s_nop 0
	v_addc_co_u32_e32 v5, vcc, 0, v3, vcc
	s_movk_i32 s0, 0x3000
	v_add_co_u32_e32 v2, vcc, s0, v2
	global_load_dwordx4 v[42:45], v[4:5], off offset:-4096 nt
	global_load_dwordx4 v[38:41], v[4:5], off nt
	v_addc_co_u32_e32 v3, vcc, 0, v3, vcc
	global_load_dwordx4 v[46:49], v[2:3], off nt
	v_lshl_add_u64 v[2:3], s[8:9], 0, v[50:51]
	v_add_co_u32_e32 v52, vcc, s4, v2
	v_lshl_add_u64 v[4:5], s[10:11], 0, v[50:51]
	s_nop 0
	v_addc_co_u32_e32 v53, vcc, 0, v3, vcc
	v_add_co_u32_e32 v54, vcc, s4, v4
	global_load_dwordx4 v[30:33], v50, s[8:9]
	global_load_dwordx4 v[26:29], v50, s[10:11]
	v_addc_co_u32_e32 v55, vcc, 0, v5, vcc
	v_add_co_u32_e32 v56, vcc, s0, v2
	v_mbcnt_lo_u32_b32 v1, -1, 0
	s_nop 0
	v_addc_co_u32_e32 v57, vcc, 0, v3, vcc
	v_add_co_u32_e32 v58, vcc, s0, v4
	v_mbcnt_hi_u32_b32 v1, -1, v1
	s_nop 0
	v_addc_co_u32_e32 v59, vcc, 0, v5, vcc
	global_load_dwordx4 v[22:25], v[52:53], off offset:-4096
	global_load_dwordx4 v[14:17], v[52:53], off
	global_load_dwordx4 v[18:21], v[54:55], off offset:-4096
	global_load_dwordx4 v[10:13], v[54:55], off
	global_load_dwordx4 v[6:9], v[56:57], off
	global_load_dwordx4 v[2:5], v[58:59], off
	v_and_b32_e32 v52, 64, v1
	v_xor_b32_e32 v53, 32, v1
	v_add_u32_e32 v52, 64, v52
	v_cmp_lt_i32_e32 vcc, v53, v52
	v_xor_b32_e32 v61, 1, v1
	v_and_b32_e32 v50, 63, v0
	v_cndmask_b32_e32 v53, v1, v53, vcc
	v_lshlrev_b32_e32 v55, 2, v53
	v_lshlrev_b32_e32 v54, 2, v0
	s_barrier
	s_waitcnt vmcnt(11)
	v_add_f32_e32 v53, v34, v35
	v_add_f32_e32 v53, v36, v53
	v_add_f32_e32 v53, v37, v53
	v_add_f32_e32 v53, 0, v53
	s_waitcnt vmcnt(10)
	v_add_f32_e32 v56, v42, v43
	s_waitcnt vmcnt(9)
	v_add_f32_e32 v57, v38, v39
	v_add_f32_e32 v56, v44, v56
	v_add_f32_e32 v57, v40, v57
	s_waitcnt vmcnt(8)
	v_add_f32_e32 v58, v46, v47
	v_add_f32_e32 v56, v45, v56
	v_add_f32_e32 v58, v48, v58
	v_add_f32_e32 v57, v41, v57
	v_add_f32_e32 v53, v53, v56
	v_add_f32_e32 v58, v49, v58
	v_add_f32_e32 v53, v53, v57
	v_add_f32_e32 v53, v53, v58
	ds_bpermute_b32 v57, v55, v53
	v_xor_b32_e32 v56, 16, v1
	v_cmp_lt_i32_e32 vcc, v56, v52
	s_waitcnt lgkmcnt(0)
	v_add_f32_e32 v53, v53, v57
	v_cndmask_b32_e32 v56, v1, v56, vcc
	v_lshlrev_b32_e32 v56, 2, v56
	ds_bpermute_b32 v58, v56, v53
	v_xor_b32_e32 v57, 8, v1
	v_cmp_lt_i32_e32 vcc, v57, v52
	s_waitcnt lgkmcnt(0)
	v_add_f32_e32 v53, v53, v58
	v_cndmask_b32_e32 v57, v1, v57, vcc
	v_lshlrev_b32_e32 v57, 2, v57
	ds_bpermute_b32 v59, v57, v53
	v_xor_b32_e32 v58, 4, v1
	v_cmp_lt_i32_e32 vcc, v58, v52
	s_waitcnt lgkmcnt(0)
	v_add_f32_e32 v53, v53, v59
	v_cndmask_b32_e32 v58, v1, v58, vcc
	v_lshlrev_b32_e32 v58, 2, v58
	ds_bpermute_b32 v60, v58, v53
	v_xor_b32_e32 v59, 2, v1
	v_cmp_lt_i32_e32 vcc, v59, v52
	s_waitcnt lgkmcnt(0)
	v_add_f32_e32 v53, v53, v60
	v_cndmask_b32_e32 v59, v1, v59, vcc
	v_lshlrev_b32_e32 v59, 2, v59
	ds_bpermute_b32 v60, v59, v53
	v_cmp_lt_i32_e32 vcc, v61, v52
	s_nop 1
	v_cndmask_b32_e32 v1, v1, v61, vcc
	v_lshlrev_b32_e32 v61, 2, v1
	s_waitcnt lgkmcnt(0)
	v_add_f32_e32 v1, v53, v60
	v_cmp_eq_u32_e32 vcc, 0, v50
	ds_bpermute_b32 v50, v61, v1
	v_lshrrev_b32_e32 v60, 4, v0
	s_and_saveexec_b64 s[0:1], vcc
	s_cbranch_execz .LBB4_2
	s_waitcnt lgkmcnt(0)
	v_add_f32_e32 v0, v1, v50
	ds_write_b32 v60, v0
